# v17 + out_odd/out_even/PP/PLE GEMMs walk their units in reverse order (start with the rows the preceding row-wise phase wrote last)
# baseline (speedup 1.0000x reference)
.LBB0_189:
	s_cmp_eq_u32 s54, 15
	v_writelane_b32 v252, s35, 12
	s_cselect_b64 s[0:1], -1, 0
	v_writelane_b32 v252, s0, 13
	s_cmp_eq_u32 s54, 14
	v_mov_b32_e32 v228, 1
	v_writelane_b32 v252, s1, 14
	s_cselect_b64 s[0:1], -1, 0
	v_writelane_b32 v252, s0, 15
	s_cmp_eq_u32 s54, 13
	v_mov_b32_e32 v222, 0x7f7f7f7f
	v_writelane_b32 v252, s1, 16
	s_cselect_b64 s[0:1], -1, 0
	v_writelane_b32 v252, s0, 17
	s_cmp_eq_u32 s54, 12
	v_mov_b32_e32 v186, 0x358637bd
	v_writelane_b32 v252, s1, 18
	s_cselect_b64 s[0:1], -1, 0
	v_writelane_b32 v252, s0, 19
	s_cmp_eq_u32 s54, 11
	v_mov_b32_e32 v224, 0x42800000
	v_writelane_b32 v252, s1, 20
	s_cselect_b64 s[0:1], -1, 0
	v_writelane_b32 v252, s0, 21
	s_cmp_eq_u32 s54, 10
	v_not_b32_e32 v225, 63
	v_writelane_b32 v252, s1, 22
	s_cselect_b64 s[0:1], -1, 0
	v_writelane_b32 v252, s0, 23
	s_cmp_eq_u32 s54, 9
	v_mov_b64_e32 v[230:231], 0x3ff
	v_writelane_b32 v252, s1, 24
	s_cselect_b64 s[0:1], -1, 0
	v_writelane_b32 v252, s0, 25
	s_cmp_eq_u32 s54, 8
	v_mov_b64_e32 v[248:249], 0x400
	v_writelane_b32 v252, s1, 26
	s_cselect_b64 s[0:1], -1, 0
	v_writelane_b32 v252, s0, 27
	s_cmp_eq_u32 s54, 7
	v_mov_b64_e32 v[250:251], 0x1ff
	v_writelane_b32 v252, s1, 28
	s_cselect_b64 s[0:1], -1, 0
	v_writelane_b32 v252, s0, 29
	s_cmp_eq_u32 s54, 6
	v_mov_b32_e32 v187, 0x4ba00000
	v_writelane_b32 v252, s1, 30
	s_cselect_b64 s[0:1], -1, 0
	v_writelane_b32 v252, s0, 31
	s_cmp_eq_u32 s54, 5
	v_mov_b32_e32 v223, 0x4b200000
	v_writelane_b32 v252, s1, 32
	s_cselect_b64 s[0:1], -1, 0
	v_writelane_b32 v252, s0, 33
	s_cmp_eq_u32 s54, 4
	v_mov_b32_e32 v229, 0xf149f2ca
	v_writelane_b32 v252, s1, 34
	s_cselect_b64 s[0:1], -1, 0
	v_writelane_b32 v252, s0, 35
	s_cmp_eq_u32 s54, 3
	s_mov_b32 s37, 0xefa18f08
	v_writelane_b32 v252, s1, 36
	s_cselect_b64 s[0:1], -1, 0
	v_writelane_b32 v252, s0, 37
	s_cmp_eq_u32 s54, 2
	s_mov_b32 s23, 0xc0e00000
	v_writelane_b32 v252, s1, 38
	s_cselect_b64 s[0:1], -1, 0
	v_writelane_b32 v252, s0, 39
	s_cmp_eq_u32 s54, 1
	s_mov_b32 s36, 0x3fb8aa3b
	v_writelane_b32 v252, s1, 40
	s_cselect_b64 s[0:1], -1, 0
	v_writelane_b32 v252, s0, 41
	s_cmp_eq_u32 s54, 0
	s_nop 0
	v_writelane_b32 v252, s1, 42
	s_cselect_b64 s[0:1], -1, 0
	v_writelane_b32 v252, s0, 43
	s_nop 1
	v_writelane_b32 v252, s1, 44
	s_lshl_b32 s0, s54, 6
	s_cmpk_lt_i32 s88, 0x100
	v_writelane_b32 v252, s0, 45
	s_cselect_b64 s[0:1], -1, 0
	v_writelane_b32 v252, s0, 46
	s_cmpk_lt_i32 s88, 0x800
	s_nop 0
	v_writelane_b32 v252, s1, 47
	s_cselect_b64 s[0:1], -1, 0
	v_writelane_b32 v252, s0, 48
	s_nop 1
	v_writelane_b32 v252, s1, 49
	s_ashr_i32 s0, s88, 31
	v_writelane_b32 v252, s0, 50
	s_lshr_b32 s0, s0, 29
	s_add_i32 s0, s88, s0
	v_readlane_b32 s1, v252, 4
	s_ashr_i32 s21, s0, 3
	s_and_b32 s0, s0, -8
	s_lshr_b32 s3, s1, 8
	s_sub_i32 s22, s88, s0
	v_writelane_b32 v252, s3, 51
	s_bfe_u32 s1, s1, 0x20006
	s_lshl_b32 s0, s22, 8
	v_writelane_b32 v252, s1, 52
	s_ashr_i32 s1, s2, 31
	s_cmpk_lt_i32 s88, 0x400
	v_writelane_b32 v252, s1, 53
	s_waitcnt lgkmcnt(0)
	s_cselect_b64 s[4:5], -1, 0
	v_writelane_b32 v252, s4, 54
	s_max_i32 s1, s2, 2
	s_and_b32 s6, s88, 1
	v_writelane_b32 v252, s5, 55
	s_lshr_b32 s4, s1, 1
	v_readlane_b32 s1, v252, 11
	s_and_b32 s1, s1, -16
	s_or_b32 s5, s1, s6
	v_writelane_b32 v252, s5, 56
	s_lshl_b32 s3, s22, 7
	v_writelane_b32 v252, s4, 57
	s_min_i32 s4, s4, 0x80
	s_cmp_gt_i32 s4, s88
	s_cselect_b64 s[4:5], -1, 0
	v_writelane_b32 v252, s4, 58
	s_nop 1
	v_writelane_b32 v252, s5, 59
	s_ashr_i32 s4, s1, 1
	s_ashr_i32 s5, s4, 31
	s_lshl_b64 s[8:9], s[4:5], 19
	v_writelane_b32 v252, s8, 60
	s_lshl_b64 s[4:5], s[4:5], 17
	s_lshl_b32 s1, s6, 17
	v_writelane_b32 v252, s9, 61
	v_writelane_b32 v252, s4, 62
	s_nop 1
	v_writelane_b32 v252, s5, 63
	s_lshr_b32 s4, s2, 31
	s_add_i32 s4, s2, s4
	s_ashr_i32 s4, s4, 1
	s_cmp_gt_i32 s2, 1
	s_cselect_b32 s4, s4, 1
	s_sub_i32 s8, s2, s4
	s_sub_i32 s9, s88, s4
	s_cmp_ge_i32 s88, s4
	s_cselect_b64 s[4:5], -1, 0
	s_and_b64 s[6:7], s[4:5], exec
	s_cselect_b32 s10, s8, 1
	s_cselect_b32 s11, s9, 0
	s_cmp_lt_i32 s2, 2
	s_cselect_b64 s[6:7], -1, 0
	s_and_b64 s[8:9], s[6:7], exec
	s_cselect_b32 s8, 1, s10
	s_cselect_b32 s9, 0, s11
	s_or_b64 s[4:5], s[6:7], s[4:5]
	s_and_b64 s[4:5], s[4:5], exec
	s_cselect_b32 s24, 0x200, 0
	s_cmp_lt_i32 s9, s24
	s_cselect_b64 s[4:5], -1, 0
	v_writelane_b32 v253, s4, 0
	s_lshr_b32 s16, s24, 3
	s_or_b32 s17, s16, 1
	v_writelane_b32 v253, s5, 1
	s_ashr_i32 s4, s9, 31
	v_writelane_b32 v253, s4, 2
	s_lshr_b32 s4, s4, 29
	s_add_i32 s4, s9, s4
	s_ashr_i32 s6, s4, 3
	s_and_b32 s4, s4, -8
	v_writelane_b32 v253, s9, 3
	s_sub_i32 s7, s9, s4
	s_ashr_i32 s4, s8, 31
	s_lshl_b32 s34, s2, 4
	v_writelane_b32 v253, s8, 4
	s_cmpk_lt_i32 s88, 0x200
	v_writelane_b32 v253, s4, 5
	s_cselect_b64 s[4:5], -1, 0
	v_writelane_b32 v253, s4, 6
	s_mul_i32 s10, s22, 0x41
	s_mul_i32 s11, s22, 5
	v_writelane_b32 v253, s5, 7
	s_lshl_b32 s4, s22, 6
	s_cmpk_lt_i32 s88, 0x180
	s_cselect_b64 s[8:9], -1, 0
	v_writelane_b32 v253, s8, 8
	s_cmp_lt_i32 s88, 32
	s_nop 0
	v_writelane_b32 v253, s9, 9
	s_cselect_b64 s[8:9], -1, 0
	v_writelane_b32 v253, s8, 10
	s_lshl_b32 s5, s22, 2
	s_nop 0
	v_writelane_b32 v253, s9, 11
	s_lshl_b32 s8, s88, 9
	v_writelane_b32 v253, s8, 12
	s_lshl_b32 s8, s2, 9
	v_writelane_b32 v253, s8, 13
	s_cmp_lt_i32 s22, 0
	s_mul_i32 s8, s22, 0x101
	s_mul_i32 s9, s22, 0x81
	s_cselect_b32 s0, s8, s0
	s_cselect_b32 s8, s9, s3
	s_cselect_b32 s9, s10, s4
	s_cselect_b32 s10, 49, 48
	s_cselect_b32 s3, s11, s5
	s_add_i32 s0, s0, s21
	s_ashr_i32 s4, s0, 31
	s_lshr_b32 s4, s4, 25
	s_add_i32 s4, s0, s4
	s_ashr_i32 s5, s0, 5
	s_and_b32 s4, s0, 31
	s_and_b32 s11, s4, 1
	s_lshr_b32 s12, s4, 1
	s_nop 0
	s_nop 0
	s_nop 0
	s_nop 0
	s_nop 0
	s_lshl_b32 s5, s5, 1
	s_nop 0
	s_nop 0
	s_add_i32 s8, s8, s21
	s_add_i32 s26, s5, s11
	s_mov_b32 s4, s12
	s_ashr_i32 s11, s8, 31
	v_writelane_b32 v253, s4, 14
	s_lshr_b32 s4, s11, 22
	s_add_i32 s4, s8, s4
	s_ashr_i32 s5, s4, 10
	s_and_b32 s4, s4, 0xfc00
	s_sub_i32 s4, s8, s4
	s_mov_b32 s0, s12
	s_sext_i32_i16 s12, s4
	s_bfe_u32 s12, s12, 0x3001c
	s_add_i32 s12, s4, s12
	s_sext_i32_i16 s13, s12
	s_and_b32 s12, s12, 0xfff8
	s_sub_i32 s12, s4, s12
	s_lshl_b32 s5, s5, 3
	s_sext_i32_i16 s12, s12
	s_lshr_b32 s4, s13, 3
	s_add_i32 s12, s5, s12
	s_ashr_i32 s5, s13, 3
	v_writelane_b32 v253, s5, 15
	s_bfe_i64 s[4:5], s[4:5], 0x100000
	s_lshl_b64 s[4:5], s[4:5], 18
	v_writelane_b32 v253, s4, 16
	s_ashr_i32 s13, s12, 31
	s_mul_i32 s10, s22, s10
	v_writelane_b32 v253, s5, 17
	s_mov_b32 s4, s12
	v_writelane_b32 v253, s4, 18
	s_nop 1
	v_writelane_b32 v253, s5, 19
	s_lshl_b64 s[4:5], s[12:13], 18
	v_writelane_b32 v253, s4, 20
	s_cmp_lt_i32 s7, 0
	s_cselect_b32 s12, s17, s16
	v_writelane_b32 v253, s5, 21
	s_lshr_b32 s4, s11, 28
	s_add_i32 s4, s8, s4
	s_and_b32 s5, s4, 0xfff0
	s_sub_i32 s5, s8, s5
	s_bfe_i32 s13, s5, 0x80000
	s_bfe_u32 s13, s13, 0x3000c
	s_mul_i32 s7, s12, s7
	s_add_i32 s13, s5, s13
	s_add_i32 s6, s7, s6
	s_add_i32 s7, s9, s21
	s_sub_i32 s7, 0x1ff, s7
	v_writelane_b32 v253, s16, 22
	s_and_b32 s16, s13, 0xf8
	s_ashr_i32 s9, s7, 31
	s_sub_i32 s16, s5, s16
	s_ashr_i32 s4, s4, 4
	s_lshr_b32 s9, s9, 27
	s_lshl_b32 s4, s4, 3
	s_sext_i32_i8 s5, s16
	s_add_i32 s9, s7, s9
	s_add_i32 s28, s4, s5
	s_and_b32 s12, s9, 0xffe0
	s_ashr_i32 s4, s28, 5
	s_sub_i32 s7, s7, s12
	s_ashr_i32 s5, s4, 31
	s_lshl_b32 s16, s16, 10
	s_bfe_i32 s12, s7, 0x80000
	s_and_b32 s16, s16, 0x1c00
	s_lshl_b64 s[4:5], s[4:5], 13
	s_bfe_u32 s12, s12, 0x3000c
	s_or_b32 s4, s4, s16
	s_bfe_u32 s16, s28, 0x20003
	s_add_i32 s12, s7, s12
	s_lshr_b32 s11, s11, 26
	s_or_b32 s4, s4, s16
	s_and_b32 s16, s12, 0xf8
	s_add_i32 s11, s8, s11
	s_sub_i32 s7, s7, s16
	s_and_b32 s16, s11, 0xffe0
	s_sub_i32 s8, s8, s16
	s_bfe_i32 s16, s8, 0x80000
	s_bfe_u32 s16, s16, 0x3000c
	s_add_i32 s16, s8, s16
	v_writelane_b32 v253, s17, 23
	s_and_b32 s17, s16, 0xfc
	s_add_i32 s10, s10, s21
	s_sub_i32 s8, s8, s17
	s_ashr_i32 s17, s10, 31
	s_lshr_b32 s17, s17, 22
	s_add_i32 s17, s10, s17
	s_and_b32 s18, s17, 0xfffffc00
	s_sub_i32 s10, s10, s18
	s_ashr_i32 s18, s6, 31
	s_lshr_b32 s18, s18, 29
	s_add_i32 s18, s6, s18
	s_and_b32 s18, s18, -8
	s_sub_i32 s20, s6, s18
	s_bfe_i32 s6, s13, 0x80000
	s_lshl_b64 s[4:5], s[4:5], 10
	s_sext_i32_i16 s6, s6
	v_writelane_b32 v253, s4, 24
	s_sext_i32_i8 s8, s8
	s_ashr_i32 s29, s28, 31
	v_writelane_b32 v253, s5, 25
	s_ashr_i32 s4, s6, 3
	v_writelane_b32 v253, s4, 26
	s_lshr_b32 s4, s6, 3
	s_bfe_i64 s[4:5], s[4:5], 0x100000
	s_lshl_b64 s[4:5], s[4:5], 18
	v_writelane_b32 v253, s4, 27
	s_sext_i32_i8 s6, s7
	s_bfe_i32 s7, s16, 0x80000
	v_writelane_b32 v253, s5, 28
	s_ashr_i32 s4, s9, 5
	s_bfe_i32 s5, s12, 0x80000
	s_lshl_b32 s4, s4, 3
	s_sext_i32_i16 s5, s5
	s_add_i32 s30, s4, s6
	s_ashr_i32 s4, s5, 3
	v_writelane_b32 v253, s4, 29
	s_ashr_i32 s6, s11, 5
	s_sext_i32_i16 s7, s7
	s_lshl_b32 s6, s6, 2
	v_writelane_b32 v253, s21, 30
	s_add_i32 s9, s3, s21
	s_ashr_i32 s3, s7, 2
	s_add_i32 s16, s6, s8
	v_writelane_b32 v253, s3, 31
	s_mov_b32 s8, s28
	v_writelane_b32 v253, s8, 32
	s_lshl_b64 s[28:29], s[28:29], 19
	s_ashr_i32 s31, s30, 31
	v_writelane_b32 v253, s9, 33
	s_ashr_i32 s6, s17, 10
	v_writelane_b32 v253, s28, 34
	s_lshr_b32 s4, s5, 3
	s_lshl_b32 s11, s6, 3
	v_writelane_b32 v253, s29, 35
	s_lshl_b64 s[28:29], s[30:31], 19
	s_sub_i32 s19, s24, s18
	s_bfe_i64 s[4:5], s[4:5], 0x100000
	s_sub_i32 s6, 3, s11
	v_writelane_b32 v253, s28, 36
	s_min_i32 s19, s19, 8
	s_min_u32 s12, s6, 8
	s_lshr_b32 s6, s7, 2
	v_writelane_b32 v253, s29, 37
	s_lshl_b64 s[28:29], s[4:5], 19
	v_writelane_b32 v253, s28, 38
	s_cmp_lt_u32 s9, 16
	v_cvt_f32_i32_e32 v1, s20
	v_writelane_b32 v253, s29, 39
	s_cselect_b64 s[28:29], -1, 0
	v_writelane_b32 v253, s28, 40
	s_ashr_i32 s8, s9, 4
	s_lshl_b32 s3, s9, 18
	v_writelane_b32 v253, s29, 41
	v_writelane_b32 v253, s9, 42
	s_ashr_i32 s9, s8, 31
	s_lshl_b64 s[8:9], s[8:9], 20
	v_writelane_b32 v253, s8, 43
	s_ashr_i32 s27, s26, 31
	s_ashr_i32 s17, s16, 31
	v_writelane_b32 v253, s9, 44
	s_lshl_b64 s[8:9], s[4:5], 18
	v_writelane_b32 v253, s8, 45
	s_lshl_b64 s[4:5], s[4:5], 17
	s_and_b32 s3, s3, 0x3c0000
	v_writelane_b32 v253, s9, 46
	v_writelane_b32 v253, s4, 47
	s_mov_b32 s29, 0
	s_mov_b32 s25, s29
	v_writelane_b32 v253, s5, 48
	s_bfe_i64 s[4:5], s[0:1], 0x100000
	s_lshl_b64 s[4:5], s[4:5], 18
	v_writelane_b32 v253, s4, 49
	s_sext_i32_i16 s0, s19
	v_cvt_f32_i32_e32 v0, s0
	v_writelane_b32 v253, s5, 50
	s_bfe_i64 s[4:5], s[6:7], 0x100000
	s_lshl_b64 s[4:5], s[4:5], 19
	v_writelane_b32 v253, s4, 51
	v_rcp_iflag_f32_e32 v2, v0
	s_mov_b32 s19, 0xf149f2ca
	v_writelane_b32 v253, s5, 52
	s_xor_b32 s4, s20, s0
	s_ashr_i32 s4, s4, 30
	s_or_b32 s6, s4, 1
	v_writelane_b32 v253, s22, 53
	s_lshr_b32 s4, s22, 31
	v_writelane_b32 v253, s4, 54
	s_lshl_b64 s[4:5], s[30:31], 18
	v_writelane_b32 v253, s4, 55
	v_mul_f32_e32 v2, v1, v2
	v_trunc_f32_e32 v2, v2
	v_writelane_b32 v253, s5, 56
	s_mov_b32 s4, s30
	v_writelane_b32 v253, s4, 57
	v_fma_f32 v1, -v2, v0, v1
	s_mov_b32 s22, 0x3d000000
	v_writelane_b32 v253, s5, 58
	s_lshl_b64 s[4:5], s[30:31], 17
	v_writelane_b32 v253, s4, 59
	s_mov_b32 s30, 0xc01d265f
	s_nop 0
	v_writelane_b32 v253, s5, 60
	s_mov_b32 s4, s26
	v_writelane_b32 v253, s4, 61
	s_nop 1
	v_writelane_b32 v253, s5, 62
	s_lshl_b64 s[4:5], s[26:27], 18
	v_writelane_b32 v253, s4, 63
	s_mov_b32 s26, 0x3b800000
	s_nop 0
	v_writelane_b32 v254, s5, 0
	s_mov_b32 s4, s16
	v_writelane_b32 v254, s4, 1
	s_nop 1
	v_writelane_b32 v254, s5, 2
	s_lshl_b64 s[4:5], s[16:17], 19
	v_writelane_b32 v254, s4, 3
	s_mov_b32 s17, 0x800000
	s_mov_b32 s16, 0x3b000000
	v_writelane_b32 v254, s5, 4
	v_cmp_ge_f32_e64 s[4:5], |v1|, |v0|
	v_cvt_i32_f32_e32 v0, v2
	s_and_b64 s[4:5], s[4:5], exec
	s_cselect_b32 s4, s6, 0
	v_cvt_f32_ubyte0_e32 v1, s12
	v_readfirstlane_b32 s5, v0
	s_add_i32 s4, s5, s4
	s_mul_i32 s4, s4, s0
	s_sub_i32 s0, s20, s4
	s_sext_i32_i16 s4, s0
	s_add_i32 s9, s18, s4
	s_ashr_i32 s4, s9, 5
	s_ashr_i32 s5, s4, 31
	s_lshl_b32 s6, s0, 10
	s_and_b32 s8, s6, 0x1c00
	s_lshl_b64 s[6:7], s[4:5], 13
	s_or_b32 s6, s6, s8
	s_bfe_u32 s8, s9, 0x20003
	s_or_b32 s6, s6, s8
	v_cvt_f32_i32_e32 v0, s10
	v_rcp_iflag_f32_e32 v2, v1
	s_lshl_b64 s[6:7], s[6:7], 10
	v_writelane_b32 v254, s6, 5
	s_lshl_b64 s[4:5], s[4:5], 22
	v_mul_f32_e32 v2, v0, v2
	v_writelane_b32 v254, s7, 6
	v_writelane_b32 v254, s4, 7
	v_trunc_f32_e32 v2, v2
	v_fma_f32 v0, -v2, v1, v0
	v_writelane_b32 v254, s5, 8
	s_lshl_b32 s4, s9, 5
	s_and_b32 s6, s4, 0x300
	s_ashr_i32 s4, s10, 30
	s_or_b32 s7, s4, 1
	v_cmp_ge_f32_e64 s[4:5], |v0|, v1
	v_cvt_i32_f32_e32 v0, v2
	s_lshl_b32 s0, s0, 18
	s_and_b32 s0, s0, 0x1c0000
	s_and_b64 s[4:5], s[4:5], exec
	s_cselect_b32 s4, s7, 0
	v_readfirstlane_b32 s5, v0
	s_add_i32 s4, s5, s4
	s_mul_i32 s5, s4, s12
	s_sub_i32 s5, s10, s5
	s_sext_i32_i16 s5, s5
	v_writelane_b32 v254, s9, 9
	s_add_i32 s5, s11, s5
	v_writelane_b32 v254, s5, 10
	s_abs_i32 s5, s2
	v_cvt_f32_u32_e32 v0, s5
	v_writelane_b32 v254, s5, 11
	s_sub_i32 s5, 0, s5
	s_sext_i32_i16 s4, s4
	v_rcp_iflag_f32_e32 v0, v0
	s_lshl_b32 s1, s1, 1
	s_lshl_b32 s0, s0, 1
	s_ashr_i32 s35, s34, 31
	v_mul_f32_e32 v0, 0x4f7ffffe, v0
	v_cvt_u32_f32_e32 v0, v0
	v_mov_b32_e32 v1, 0
	s_add_i32 s31, 0, 0x23600
	s_mov_b32 s18, 0xbd38aa3b
	v_readfirstlane_b32 s7, v0
	s_mul_i32 s5, s5, s7
	s_mul_hi_u32 s5, s7, s5
	s_add_i32 s5, s7, s5
	v_writelane_b32 v254, s5, 12
	v_writelane_b32 v254, s24, 13
	s_nop 1
	v_writelane_b32 v254, s25, 14
	v_writelane_b32 v254, s4, 15
	v_writelane_b32 v254, s1, 16
	v_writelane_b32 v254, s0, 17
	s_lshl_b32 s0, s6, 1
	v_writelane_b32 v254, s0, 18
	s_lshl_b32 s0, s3, 1
	v_writelane_b32 v254, s0, 19
	s_lshl_b32 s0, s88, 7
	v_writelane_b32 v254, s0, 20
	s_lshl_b32 s0, s2, 7
	v_writelane_b32 v254, s0, 21
	s_lshl_b32 s0, s88, 5
	v_writelane_b32 v254, s0, 22
	s_lshl_b32 s0, s2, 5
	v_writelane_b32 v254, s0, 23
	s_add_i32 s0, 0, 0x22000
	v_writelane_b32 v254, s0, 24
	s_add_i32 s0, 0, 0x22004
	v_writelane_b32 v254, s0, 25
	s_add_i32 s0, 0, 0x22d10
	v_writelane_b32 v254, s0, 26
	s_add_i32 s0, 0, 0x22d20
	v_writelane_b32 v254, s0, 27
	s_add_i32 s0, 0, 0x22d30
	v_writelane_b32 v254, s0, 28
	s_add_i32 s0, 0, 0x22d40
	v_writelane_b32 v254, s0, 29
	s_add_i32 s0, 0, 0x22d50
	v_writelane_b32 v254, s0, 30
	s_add_i32 s0, 0, 0x22d60
	v_writelane_b32 v254, s0, 31
	s_add_i32 s0, 0, 0x22d70
	v_writelane_b32 v254, s0, 32
	s_add_i32 s0, 0, 0x22500
	v_writelane_b32 v254, s0, 33
	s_add_i32 s0, 0, 0x23500
	v_writelane_b32 v254, s0, 34
	s_add_i32 s0, 0, 0x22d80
	v_writelane_b32 v254, s0, 35
	s_add_i32 s0, 0, 0x22d90
	v_writelane_b32 v254, s0, 36
	s_add_i32 s0, 0, 0x22da0
	v_writelane_b32 v254, s0, 37
	s_add_i32 s0, 0, 0x22db0
	v_writelane_b32 v254, s0, 38
	s_add_i32 s0, 0, 0x22dc0
	v_writelane_b32 v254, s0, 39
	s_add_i32 s0, 0, 0x22dd0
	v_writelane_b32 v254, s0, 40
	s_add_i32 s0, 0, 0x22de0
	v_writelane_b32 v254, s0, 41
	s_add_i32 s0, 0, 0x22df0
	v_writelane_b32 v254, s0, 42
	s_add_i32 s0, 0, 0x22100
	v_writelane_b32 v254, s0, 43
	s_add_i32 s0, 0, 0x23510
	v_writelane_b32 v254, s0, 44
	s_add_i32 s0, 0, 0x23610
	v_writelane_b32 v254, s0, 45
	s_add_i32 s0, 0, 0x23520
	v_writelane_b32 v254, s0, 46
	s_add_i32 s0, 0, 0x23620
	v_writelane_b32 v254, s0, 47
	s_add_i32 s0, 0, 0x23530
	v_writelane_b32 v254, s0, 48
	s_add_i32 s0, 0, 0x23630
	v_writelane_b32 v254, s0, 49
	s_add_i32 s0, 0, 0x23540
	v_writelane_b32 v254, s0, 50
	s_add_i32 s0, 0, 0x23640
	v_writelane_b32 v254, s0, 51
	s_add_i32 s0, 0, 0x23550
	v_writelane_b32 v254, s0, 52
	s_add_i32 s0, 0, 0x23650
	v_writelane_b32 v254, s0, 53
	s_add_i32 s0, 0, 0x23560
	v_writelane_b32 v254, s0, 54
	s_add_i32 s0, 0, 0x23660
	v_writelane_b32 v254, s0, 55
	s_add_i32 s0, 0, 0x23570
	v_writelane_b32 v254, s0, 56
	s_add_i32 s0, 0, 0x23670
	v_writelane_b32 v254, s0, 57
	s_add_i32 s0, 0, 0x23680
	v_writelane_b32 v254, s0, 58
	s_lshl_b64 s[4:5], s[34:35], 11
	v_writelane_b32 v254, s4, 59
	s_movk_i32 s1, 0x200
	s_add_i32 s3, 0, 0x24a00
	v_writelane_b32 v254, s5, 60
	s_lshl_b64 s[4:5], s[34:35], 10
	v_writelane_b32 v254, s4, 61
	s_mov_b64 s[24:25], 0x80
	s_mov_b32 s0, 0x3e000000
	v_writelane_b32 v254, s5, 62
	s_mov_b32 s4, s88
	v_writelane_b32 v254, s4, 63
	s_mov_b32 s6, s29
	s_nop 0
	v_writelane_b32 v255, s5, 0
	v_writelane_b32 v255, s34, 1
	s_nop 1
	v_writelane_b32 v255, s35, 2
	s_branch .LBB0_193

.LBB0_832:
	s_ashr_i32 s12, s20, 3
	s_add_i32 s12, s42, s12
	s_sub_i32 s12, 0x1ff, s12
	s_ashr_i32 s13, s12, 31
	s_lshr_b32 s13, s13, 27
	s_add_i32 s13, s12, s13
	s_ashr_i32 s20, s13, 5
	s_lshl_b32 s20, s20, 3
	s_sub_i32 s21, 0x80, s20
	s_min_i32 s21, s21, 8
	s_abs_i32 s42, s21
	v_cvt_f32_u32_e32 v0, s42
	s_sub_i32 s48, 0, s42
	s_andn2_b32 s13, s13, 31
	s_sub_i32 s13, s12, s13
	v_rcp_iflag_f32_e32 v0, v0
	s_abs_i32 s12, s13
	s_xor_b32 s43, s13, s21
	s_ashr_i32 s43, s43, 31
	v_mul_f32_e32 v0, 0x4f7ffffe, v0
	v_cvt_u32_f32_e32 v0, v0
	s_nop 0
	v_readfirstlane_b32 s49, v0
	s_mul_i32 s48, s48, s49
	s_mul_hi_u32 s48, s49, s48
	s_add_i32 s49, s49, s48
	s_mul_hi_u32 s48, s12, s49
	s_mul_i32 s49, s48, s42
	s_sub_i32 s12, s12, s49
	s_add_i32 s71, s48, 1
	s_sub_i32 s49, s12, s42
	s_cmp_ge_u32 s12, s42
	s_cselect_b32 s48, s71, s48
	s_cselect_b32 s12, s49, s12
	s_add_i32 s49, s48, 1
	s_cmp_ge_u32 s12, s42
	s_cselect_b32 s12, s49, s48
	s_xor_b32 s12, s12, s43
	s_sub_i32 s12, s12, s43
	s_mul_i32 s21, s12, s21
	s_sub_i32 s13, s13, s21
	s_add_i32 s20, s20, s13

.LBB0_1473:
	s_ashr_i32 s12, s14, 3
	s_add_i32 s12, s34, s12
	s_sub_i32 s12, 0x1ff, s12
	s_ashr_i32 s13, s12, 31
	s_lshr_b32 s13, s13, 27
	s_add_i32 s13, s12, s13
	s_ashr_i32 s14, s13, 5
	s_lshl_b32 s14, s14, 3
	s_sub_i32 s15, 0x80, s14
	s_min_i32 s15, s15, 8
	s_abs_i32 s34, s15
	v_cvt_f32_u32_e32 v0, s34
	s_sub_i32 s42, 0, s34
	s_andn2_b32 s13, s13, 31
	s_sub_i32 s13, s12, s13
	v_rcp_iflag_f32_e32 v0, v0
	s_abs_i32 s12, s13
	s_xor_b32 s35, s13, s15
	s_ashr_i32 s35, s35, 31
	v_mul_f32_e32 v0, 0x4f7ffffe, v0
	v_cvt_u32_f32_e32 v0, v0
	s_nop 0
	v_readfirstlane_b32 s43, v0
	s_mul_i32 s42, s42, s43
	s_mul_hi_u32 s42, s43, s42
	s_add_i32 s43, s43, s42
	s_mul_hi_u32 s42, s12, s43
	s_mul_i32 s43, s42, s34
	s_sub_i32 s12, s12, s43
	s_add_i32 s65, s42, 1
	s_sub_i32 s43, s12, s34
	s_cmp_ge_u32 s12, s34
	s_cselect_b32 s42, s65, s42
	s_cselect_b32 s12, s43, s12
	s_add_i32 s43, s42, 1
	s_cmp_ge_u32 s12, s34
	s_cselect_b32 s12, s43, s42
	s_xor_b32 s12, s12, s35
	s_sub_i32 s12, s12, s35
	s_mul_i32 s15, s12, s15
	s_sub_i32 s13, s13, s15
	s_add_i32 s14, s14, s13

.LBB0_1716:
	s_ashr_i32 s6, s8, 3
	s_add_i32 s6, s20, s6
	s_sub_i32 s6, 0x1ff, s6
	s_ashr_i32 s7, s6, 31
	s_lshr_b32 s7, s7, 27
	s_add_i32 s7, s6, s7
	s_ashr_i32 s8, s7, 5
	s_lshl_b32 s8, s8, 3
	s_sub_i32 s9, 0x80, s8
	s_min_i32 s9, s9, 8
	s_abs_i32 s20, s9
	v_cvt_f32_u32_e32 v0, s20
	s_sub_i32 s35, 0, s20
	s_andn2_b32 s7, s7, 31
	s_sub_i32 s7, s6, s7
	v_rcp_iflag_f32_e32 v0, v0
	s_abs_i32 s6, s7
	s_xor_b32 s21, s7, s9
	s_ashr_i32 s21, s21, 31
	v_mul_f32_e32 v0, 0x4f7ffffe, v0
	v_cvt_u32_f32_e32 v0, v0
	s_nop 0
	v_readfirstlane_b32 s38, v0
	s_mul_i32 s35, s35, s38
	s_mul_hi_u32 s35, s38, s35
	s_add_i32 s38, s38, s35
	s_mul_hi_u32 s35, s6, s38
	s_mul_i32 s38, s35, s20
	s_sub_i32 s6, s6, s38
	s_add_i32 s39, s35, 1
	s_sub_i32 s38, s6, s20
	s_cmp_ge_u32 s6, s20
	s_cselect_b32 s35, s39, s35
	s_cselect_b32 s6, s38, s6
	s_add_i32 s38, s35, 1
	s_cmp_ge_u32 s6, s20
	s_cselect_b32 s6, s38, s35
	s_xor_b32 s6, s6, s21
	s_sub_i32 s6, s6, s21
	s_mul_i32 s9, s6, s9
	s_sub_i32 s7, s7, s9
	s_add_i32 s8, s8, s7

.LBB0_1923:
	s_ashr_i32 s14, s20, 3
	s_add_i32 s14, s38, s14
	s_sub_i32 s14, 0x1ff, s14
	s_ashr_i32 s15, s14, 31
	s_lshr_b32 s15, s15, 27
	s_add_i32 s15, s14, s15
	s_ashr_i32 s20, s15, 5
	s_lshl_b32 s20, s20, 3
	s_sub_i32 s21, 0x80, s20
	s_min_i32 s21, s21, 8
	s_abs_i32 s38, s21
	v_cvt_f32_u32_e32 v0, s38
	s_sub_i32 s42, 0, s38
	s_andn2_b32 s15, s15, 31
	s_sub_i32 s15, s14, s15
	v_rcp_iflag_f32_e32 v0, v0
	s_abs_i32 s14, s15
	s_xor_b32 s39, s15, s21
	s_ashr_i32 s39, s39, 31
	v_mul_f32_e32 v0, 0x4f7ffffe, v0
	v_cvt_u32_f32_e32 v0, v0
	s_nop 0
	v_readfirstlane_b32 s43, v0
	s_mul_i32 s42, s42, s43
	s_mul_hi_u32 s42, s43, s42
	s_add_i32 s43, s43, s42
	s_mul_hi_u32 s42, s14, s43
	s_mul_i32 s43, s42, s38
	s_sub_i32 s14, s14, s43
	s_add_i32 s67, s42, 1
	s_sub_i32 s43, s14, s38
	s_cmp_ge_u32 s14, s38
	s_cselect_b32 s42, s67, s42
	s_cselect_b32 s14, s43, s14
	s_add_i32 s43, s42, 1
	s_cmp_ge_u32 s14, s38
	s_cselect_b32 s14, s43, s42
	s_xor_b32 s14, s14, s39
	s_sub_i32 s14, s14, s39
	s_mul_i32 s21, s14, s21
	s_sub_i32 s15, s15, s21
	s_add_i32 s20, s20, s15
